# speedup vs baseline: 1.0326x; 1.0046x over previous
.Lmy_wg_skip:
	s_or_b64 exec, exec, s[16:17]
	global_load_dwordx4 v[44:47], v[20:21], off offset:144
	global_load_dwordx4 v[56:59], v[20:21], off offset:128
	global_load_dwordx4 v[0:3], v[20:21], off offset:208
	global_load_dwordx4 v[8:11], v[20:21], off offset:192
	global_load_dwordx4 v[4:7], v[20:21], off offset:272
	global_load_dwordx4 v[12:15], v[20:21], off offset:256
	v_lshl_add_u64 v[16:17], s[8:9], 0, v[72:73]
	v_lshlrev_b32_e32 v72, 4, v141
	v_lshl_add_u64 v[16:17], v[16:17], 0, v[72:73]
	v_mad_u32_u24 v74, v76, s4, v72
	global_load_dwordx4 v[156:159], v[16:17], off
	global_load_dwordx4 v[152:155], v[16:17], off offset:32
	global_load_dwordx4 v[148:151], v[16:17], off offset:64
	global_load_dwordx4 v[144:147], v[16:17], off offset:96
	global_load_dwordx4 v[32:35], v[20:21], off offset:336
	global_load_dwordx4 v[36:39], v[20:21], off offset:320
	global_load_dwordx4 v[24:27], v[20:21], off offset:400
	global_load_dwordx4 v[28:31], v[20:21], off offset:384
	s_nop 0
	global_load_dwordx4 v[16:19], v[20:21], off offset:464
	s_nop 0
	global_load_dwordx4 v[20:23], v[20:21], off offset:448
	s_waitcnt lgkmcnt(0)
	s_barrier
	ds_read_b128 v[68:71], v74
	s_mov_b32 s3, 0x43800000
	v_fma_mix_f32 v143, v64, s3, -v60 op_sel_hi:[0,0,1]
	v_fma_mix_f32 v160, v65, s3, -v60 op_sel:[0,0,1] op_sel_hi:[0,0,1]
	v_fma_mix_f32 v161, v66, s3, -v61 op_sel_hi:[0,0,1]
	v_fma_mix_f32 v162, v67, s3, -v61 op_sel:[0,0,1] op_sel_hi:[0,0,1]
	ds_read_b128 v[64:67], v74 offset:32
	s_waitcnt lgkmcnt(1)
	v_mfma_f32_32x32x16_f16 a[16:31], v[60:63], v[68:71], 0
	v_fma_mix_f32 v163, v40, s3, -v62 op_sel_hi:[0,0,1]
	v_fma_mix_f32 v43, v43, s3, -v63 op_sel:[0,0,1] op_sel_hi:[0,0,1]
	v_fma_mix_f32 v164, v41, s3, -v62 op_sel:[0,0,1] op_sel_hi:[0,0,1]
	v_fma_mix_f32 v165, v42, s3, -v63 op_sel_hi:[0,0,1]
	v_cvt_pk_f16_f32 v40, v143, v160
	v_cvt_pk_f16_f32 v41, v161, v162
	v_cvt_pk_f16_f32 v42, v163, v164
	v_cvt_pk_f16_f32 v43, v165, v43
	s_nop 0
	v_mfma_f32_32x32x16_f16 a[16:31], v[40:43], v[68:71], a[16:31]
	ds_read_b128 v[68:71], v74 offset:8704
	ds_read_b128 v[160:163], v74 offset:8736
	s_waitcnt lgkmcnt(1)
	v_mfma_f32_32x32x16_f16 a[0:15], v[60:63], v[68:71], 0
	v_mfma_f32_32x32x16_f16 a[0:15], v[40:43], v[68:71], a[0:15]
	v_mov_b32_e32 v40, 0x4400
	v_mad_u32_u24 v41, v76, s4, v40
	v_add_u32_e32 v40, v41, v72
	ds_read_b128 v[68:71], v40
	ds_read_b128 v[164:167], v40 offset:32
	s_waitcnt vmcnt(18)
	v_mul_f32_e32 v42, 0x43800000, v52
	v_mul_f32_e32 v43, 0x43800000, v53
	s_waitcnt lgkmcnt(1)
	v_mfma_f32_32x32x16_f16 a[16:31], v[60:63], v[68:71], a[16:31]
	ds_read_b128 v[68:71], v40 offset:8704
	ds_read_b128 v[168:171], v40 offset:8736
	s_waitcnt lgkmcnt(1)
	v_mfma_f32_32x32x16_f16 a[0:15], v[60:63], v[68:71], a[0:15]
	v_mul_f32_e32 v61, 0x43800000, v54
	v_mul_f32_e32 v62, 0x43800000, v55
	v_cvt_pk_f16_f32 v60, v42, v43
	v_cvt_pk_f16_f32 v61, v61, v62
	s_nop 0
	v_fma_mix_f32 v42, v52, s3, -v60 op_sel_hi:[0,0,1]
	v_fma_mix_f32 v43, v53, s3, -v60 op_sel:[0,0,1] op_sel_hi:[0,0,1]
	v_fma_mix_f32 v52, v54, s3, -v61 op_sel_hi:[0,0,1]
	v_fma_mix_f32 v53, v55, s3, -v61 op_sel:[0,0,1] op_sel_hi:[0,0,1]
	s_waitcnt vmcnt(17)
	v_mul_f32_e32 v54, 0x43800000, v48
	v_mul_f32_e32 v55, 0x43800000, v49
	v_cvt_pk_f16_f32 v62, v54, v55
	v_mul_f32_e32 v54, 0x43800000, v50
	v_mul_f32_e32 v55, 0x43800000, v51
	v_cvt_pk_f16_f32 v63, v54, v55
	v_fma_mix_f32 v54, v48, s3, -v62 op_sel_hi:[0,0,1]
	v_mfma_f32_32x32x16_f16 a[16:31], v[60:63], v[64:67], a[16:31]
	v_fma_mix_f32 v51, v51, s3, -v63 op_sel:[0,0,1] op_sel_hi:[0,0,1]
	v_fma_mix_f32 v55, v49, s3, -v62 op_sel:[0,0,1] op_sel_hi:[0,0,1]
	v_fma_mix_f32 v68, v50, s3, -v63 op_sel_hi:[0,0,1]
	v_cvt_pk_f16_f32 v48, v42, v43
	v_cvt_pk_f16_f32 v49, v52, v53
	v_cvt_pk_f16_f32 v50, v54, v55
	v_cvt_pk_f16_f32 v51, v68, v51
	v_mfma_f32_32x32x16_f16 a[0:15], v[60:63], v[160:163], a[0:15]
	ds_read_b128 v[52:55], v74 offset:64
	s_waitcnt vmcnt(14)
	v_mul_f32_e32 v42, 0x43800000, v56
	v_mul_f32_e32 v43, 0x43800000, v57
	v_mfma_f32_32x32x16_f16 a[16:31], v[48:51], v[64:67], a[16:31]
	v_mfma_f32_32x32x16_f16 a[0:15], v[48:51], v[160:163], a[0:15]
	v_mul_f32_e32 v49, 0x43800000, v58
	v_mul_f32_e32 v50, 0x43800000, v59
	v_cvt_pk_f16_f32 v49, v49, v50
	v_mul_f32_e32 v50, 0x43800000, v44
	v_mul_f32_e32 v51, 0x43800000, v45
	v_cvt_pk_f16_f32 v48, v42, v43
	v_cvt_pk_f16_f32 v50, v50, v51
	v_mfma_f32_32x32x16_f16 a[16:31], v[60:63], v[164:167], a[16:31]
	v_fma_mix_f32 v42, v56, s3, -v48 op_sel_hi:[0,0,1]
	v_mul_f32_e32 v51, 0x43800000, v46
	v_mul_f32_e32 v56, 0x43800000, v47
	v_fma_mix_f32 v43, v57, s3, -v48 op_sel:[0,0,1] op_sel_hi:[0,0,1]
	v_cvt_pk_f16_f32 v51, v51, v56
	v_fma_mix_f32 v44, v44, s3, -v50 op_sel_hi:[0,0,1]
	v_fma_mix_f32 v45, v45, s3, -v50 op_sel:[0,0,1] op_sel_hi:[0,0,1]
	s_waitcnt lgkmcnt(1)
	v_mfma_f32_32x32x16_f16 a[0:15], v[60:63], v[168:171], a[0:15]
	v_fma_mix_f32 v60, v58, s3, -v49 op_sel_hi:[0,0,1]
	v_fma_mix_f32 v61, v59, s3, -v49 op_sel:[0,0,1] op_sel_hi:[0,0,1]
	ds_read_b128 v[56:59], v74 offset:96
	v_fma_mix_f32 v46, v46, s3, -v51 op_sel_hi:[0,0,1]
	v_fma_mix_f32 v47, v47, s3, -v51 op_sel:[0,0,1] op_sel_hi:[0,0,1]
	v_cvt_pk_f16_f32 v42, v42, v43
	v_cvt_pk_f16_f32 v43, v60, v61
	s_waitcnt lgkmcnt(1)
	v_mfma_f32_32x32x16_f16 a[16:31], v[48:51], v[52:55], a[16:31]
	v_cvt_pk_f16_f32 v44, v44, v45
	v_cvt_pk_f16_f32 v45, v46, v47
	s_waitcnt vmcnt(13)
	v_mul_f32_e32 v46, 0x43800000, v3
	v_mfma_f32_32x32x16_f16 a[16:31], v[42:45], v[52:55], a[16:31]
	ds_read_b128 v[52:55], v74 offset:8768
	ds_read_b128 v[60:63], v74 offset:8800
	s_waitcnt lgkmcnt(1)
	v_mfma_f32_32x32x16_f16 a[0:15], v[48:51], v[52:55], a[0:15]
	v_mfma_f32_32x32x16_f16 a[0:15], v[42:45], v[52:55], a[0:15]
	ds_read_b128 v[42:45], v40 offset:64
	ds_read_b128 v[52:55], v40 offset:96
	s_waitcnt lgkmcnt(1)
	v_mfma_f32_32x32x16_f16 a[16:31], v[48:51], v[42:45], a[16:31]
	ds_read_b128 v[42:45], v40 offset:8768
	ds_read_b128 v[64:67], v40 offset:8800
	s_waitcnt lgkmcnt(1)
	v_mfma_f32_32x32x16_f16 a[0:15], v[48:51], v[42:45], a[0:15]
	s_waitcnt vmcnt(12)
	v_mul_f32_e32 v42, 0x43800000, v8
	v_mul_f32_e32 v43, 0x43800000, v9
	v_mul_f32_e32 v44, 0x43800000, v10
	v_mul_f32_e32 v45, 0x43800000, v11
	v_cvt_pk_f16_f32 v42, v42, v43
	v_cvt_pk_f16_f32 v43, v44, v45
	v_mul_f32_e32 v44, 0x43800000, v0
	v_mul_f32_e32 v45, 0x43800000, v1
	v_cvt_pk_f16_f32 v44, v44, v45
	v_mul_f32_e32 v45, 0x43800000, v2
	v_cvt_pk_f16_f32 v45, v45, v46
	v_fma_mix_f32 v8, v8, s3, -v42 op_sel_hi:[0,0,1]
	v_fma_mix_f32 v3, v3, s3, -v45 op_sel:[0,0,1] op_sel_hi:[0,0,1]
	v_mfma_f32_32x32x16_f16 a[16:31], v[42:45], v[56:59], a[16:31]
	v_fma_mix_f32 v9, v9, s3, -v42 op_sel:[0,0,1] op_sel_hi:[0,0,1]
	v_fma_mix_f32 v10, v10, s3, -v43 op_sel_hi:[0,0,1]
	v_fma_mix_f32 v11, v11, s3, -v43 op_sel:[0,0,1] op_sel_hi:[0,0,1]
	v_fma_mix_f32 v46, v0, s3, -v44 op_sel_hi:[0,0,1]
	v_fma_mix_f32 v47, v1, s3, -v44 op_sel:[0,0,1] op_sel_hi:[0,0,1]
	v_fma_mix_f32 v48, v2, s3, -v45 op_sel_hi:[0,0,1]
	v_cvt_pk_f16_f32 v0, v8, v9
	v_cvt_pk_f16_f32 v1, v10, v11
	v_cvt_pk_f16_f32 v2, v46, v47
	v_cvt_pk_f16_f32 v3, v48, v3
	s_waitcnt vmcnt(10)
	v_mul_f32_e32 v8, 0x43800000, v12
	v_mfma_f32_32x32x16_f16 a[16:31], v[0:3], v[56:59], a[16:31]
	v_mul_f32_e32 v9, 0x43800000, v13
	v_mul_f32_e32 v10, 0x43800000, v14
	v_mul_f32_e32 v11, 0x43800000, v15
	v_cvt_pk_f16_f32 v8, v8, v9
	v_cvt_pk_f16_f32 v9, v10, v11
	v_mul_f32_e32 v10, 0x43800000, v4
	v_fma_mix_f32 v50, v12, s3, -v8 op_sel_hi:[0,0,1]
	v_mfma_f32_32x32x16_f16 a[16:31], v[42:45], v[52:55], a[16:31]
	v_fma_mix_f32 v51, v13, s3, -v8 op_sel:[0,0,1] op_sel_hi:[0,0,1]
	v_fma_mix_f32 v52, v14, s3, -v9 op_sel_hi:[0,0,1]
	v_fma_mix_f32 v53, v15, s3, -v9 op_sel:[0,0,1] op_sel_hi:[0,0,1]
	ds_read_b128 v[12:15], v74 offset:128
	v_mul_f32_e32 v11, 0x43800000, v5
	v_cvt_pk_f16_f32 v10, v10, v11
	v_mul_f32_e32 v11, 0x43800000, v6
	v_mul_f32_e32 v46, 0x43800000, v7
	v_cvt_pk_f16_f32 v11, v11, v46
	ds_read_b128 v[46:49], v74 offset:160
	s_waitcnt lgkmcnt(1)
	v_mfma_f32_32x32x16_f16 a[16:31], v[8:11], v[12:15], a[16:31]
	v_fma_mix_f32 v7, v7, s3, -v11 op_sel:[0,0,1] op_sel_hi:[0,0,1]
	v_fma_mix_f32 v54, v4, s3, -v10 op_sel_hi:[0,0,1]
	v_fma_mix_f32 v55, v5, s3, -v10 op_sel:[0,0,1] op_sel_hi:[0,0,1]
	v_fma_mix_f32 v56, v6, s3, -v11 op_sel_hi:[0,0,1]
	v_cvt_pk_f16_f32 v4, v50, v51
	v_cvt_pk_f16_f32 v5, v52, v53
	v_cvt_pk_f16_f32 v6, v54, v55
	v_cvt_pk_f16_f32 v7, v56, v7
	s_waitcnt vmcnt(5)
	v_mul_f32_e32 v54, 0x43800000, v35
	v_mfma_f32_32x32x16_f16 a[16:31], v[4:7], v[12:15], a[16:31]
	ds_read_b128 v[12:15], v40 offset:128
	ds_read_b128 v[50:53], v40 offset:160
	v_mul_f32_e32 v57, 0x43800000, v135
	s_waitcnt lgkmcnt(1)
	v_mfma_f32_32x32x16_f16 a[16:31], v[8:11], v[12:15], a[16:31]
	s_waitcnt vmcnt(4)
	v_mul_f32_e32 v12, 0x43800000, v36
	v_mul_f32_e32 v13, 0x43800000, v37
	v_mul_f32_e32 v14, 0x43800000, v38
	v_mul_f32_e32 v15, 0x43800000, v39
	v_cvt_pk_f16_f32 v12, v12, v13
	v_cvt_pk_f16_f32 v13, v14, v15
	v_mul_f32_e32 v14, 0x43800000, v32
	v_mul_f32_e32 v15, 0x43800000, v33
	v_cvt_pk_f16_f32 v14, v14, v15
	v_mul_f32_e32 v15, 0x43800000, v34
	v_cvt_pk_f16_f32 v15, v15, v54
	v_fma_mix_f32 v36, v36, s3, -v12 op_sel_hi:[0,0,1]
	v_fma_mix_f32 v35, v35, s3, -v15 op_sel:[0,0,1] op_sel_hi:[0,0,1]
	v_mfma_f32_32x32x16_f16 a[16:31], v[12:15], v[46:49], a[16:31]
	v_fma_mix_f32 v37, v37, s3, -v12 op_sel:[0,0,1] op_sel_hi:[0,0,1]
	v_fma_mix_f32 v38, v38, s3, -v13 op_sel_hi:[0,0,1]
	v_fma_mix_f32 v39, v39, s3, -v13 op_sel:[0,0,1] op_sel_hi:[0,0,1]
	v_fma_mix_f32 v54, v32, s3, -v14 op_sel_hi:[0,0,1]
	v_fma_mix_f32 v55, v33, s3, -v14 op_sel:[0,0,1] op_sel_hi:[0,0,1]
	v_fma_mix_f32 v56, v34, s3, -v15 op_sel_hi:[0,0,1]
	v_cvt_pk_f16_f32 v32, v36, v37
	v_cvt_pk_f16_f32 v33, v38, v39
	v_cvt_pk_f16_f32 v34, v54, v55
	v_cvt_pk_f16_f32 v35, v56, v35
	s_waitcnt vmcnt(2)
	v_mul_f32_e32 v36, 0x43800000, v28
	v_mfma_f32_32x32x16_f16 a[16:31], v[32:35], v[46:49], a[16:31]
	v_mul_f32_e32 v37, 0x43800000, v29
	v_mul_f32_e32 v38, 0x43800000, v30
	v_mul_f32_e32 v39, 0x43800000, v31
	v_cvt_pk_f16_f32 v36, v36, v37
	v_cvt_pk_f16_f32 v37, v38, v39
	v_mul_f32_e32 v38, 0x43800000, v24
	v_mul_f32_e32 v39, 0x43800000, v25
	s_waitcnt lgkmcnt(0)
	v_mfma_f32_32x32x16_f16 a[16:31], v[12:15], v[50:53], a[16:31]
	v_fma_mix_f32 v50, v28, s3, -v36 op_sel_hi:[0,0,1]
	v_fma_mix_f32 v51, v29, s3, -v36 op_sel:[0,0,1] op_sel_hi:[0,0,1]
	v_fma_mix_f32 v52, v30, s3, -v37 op_sel_hi:[0,0,1]
	v_fma_mix_f32 v53, v31, s3, -v37 op_sel:[0,0,1] op_sel_hi:[0,0,1]
	ds_read_b128 v[28:31], v74 offset:192
	v_cvt_pk_f16_f32 v38, v38, v39
	v_mul_f32_e32 v39, 0x43800000, v26
	v_mul_f32_e32 v46, 0x43800000, v27
	v_mfma_f32_32x32x16_f16 a[0:15], v[42:45], v[60:63], a[0:15]
	v_cvt_pk_f16_f32 v39, v39, v46
	ds_read_b128 v[46:49], v74 offset:224
	v_fma_mix_f32 v27, v27, s3, -v39 op_sel:[0,0,1] op_sel_hi:[0,0,1]
	v_fma_mix_f32 v54, v24, s3, -v38 op_sel_hi:[0,0,1]
	v_fma_mix_f32 v55, v25, s3, -v38 op_sel:[0,0,1] op_sel_hi:[0,0,1]
	v_fma_mix_f32 v56, v26, s3, -v39 op_sel_hi:[0,0,1]
	v_cvt_pk_f16_f32 v24, v50, v51
	s_waitcnt lgkmcnt(1)
	v_mfma_f32_32x32x16_f16 a[16:31], v[36:39], v[28:31], a[16:31]
	v_cvt_pk_f16_f32 v25, v52, v53
	v_cvt_pk_f16_f32 v26, v54, v55
	v_cvt_pk_f16_f32 v27, v56, v27
	s_waitcnt vmcnt(1)
	v_mul_f32_e32 v54, 0x43800000, v19
	v_mfma_f32_32x32x16_f16 a[0:15], v[0:3], v[60:63], a[0:15]
	v_mfma_f32_32x32x16_f16 a[16:31], v[24:27], v[28:31], a[16:31]
	ds_read_b128 v[28:31], v40 offset:192
	ds_read_b128 v[50:53], v40 offset:224
	v_mfma_f32_32x32x16_f16 a[0:15], v[42:45], v[64:67], a[0:15]
	v_mov_b32_e32 v44, v158
	v_mov_b32_e32 v42, v159
	s_waitcnt lgkmcnt(1)
	v_mfma_f32_32x32x16_f16 a[16:31], v[36:39], v[28:31], a[16:31]
	s_waitcnt vmcnt(0)
	v_mul_f32_e32 v28, 0x43800000, v20
	v_mul_f32_e32 v29, 0x43800000, v21
	v_mul_f32_e32 v30, 0x43800000, v22
	v_mul_f32_e32 v31, 0x43800000, v23
	v_cvt_pk_f16_f32 v28, v28, v29
	v_cvt_pk_f16_f32 v29, v30, v31
	v_mul_f32_e32 v30, 0x43800000, v16
	v_mul_f32_e32 v31, 0x43800000, v17
	v_fma_mix_f32 v20, v20, s3, -v28 op_sel_hi:[0,0,1]
	v_fma_mix_f32 v21, v21, s3, -v28 op_sel:[0,0,1] op_sel_hi:[0,0,1]
	v_fma_mix_f32 v22, v22, s3, -v29 op_sel_hi:[0,0,1]
	v_fma_mix_f32 v23, v23, s3, -v29 op_sel:[0,0,1] op_sel_hi:[0,0,1]
	v_cvt_pk_f16_f32 v30, v30, v31
	v_mul_f32_e32 v31, 0x43800000, v18
	v_cvt_pk_f16_f32 v31, v31, v54
	v_fma_mix_f32 v54, v16, s3, -v30 op_sel_hi:[0,0,1]
	v_fma_mix_f32 v55, v17, s3, -v30 op_sel:[0,0,1] op_sel_hi:[0,0,1]
	v_cvt_pk_f16_f32 v16, v20, v21
	v_cvt_pk_f16_f32 v17, v22, v23
	ds_read_b128 v[0:3], v74 offset:8832
	ds_read_b128 v[20:23], v74 offset:8864
	s_waitcnt lgkmcnt(1)
	v_mfma_f32_32x32x16_f16 a[0:15], v[8:11], v[0:3], a[0:15]
	v_fma_mix_f32 v19, v19, s3, -v31 op_sel:[0,0,1] op_sel_hi:[0,0,1]
	v_fma_mix_f32 v56, v18, s3, -v31 op_sel_hi:[0,0,1]
	v_cvt_pk_f16_f32 v18, v54, v55
	v_cvt_pk_f16_f32 v19, v56, v19
	v_mul_f32_e32 v54, 0x43800000, v139
	v_mul_f32_e32 v55, 0x43800000, v133
	v_mul_f32_e32 v56, 0x43800000, v134
	v_mfma_f32_32x32x16_f16 a[0:15], v[4:7], v[0:3], a[0:15]
	ds_read_b128 v[0:3], v40 offset:8832
	ds_read_b128 v[4:7], v40 offset:8864
	s_waitcnt lgkmcnt(1)
	v_mfma_f32_32x32x16_f16 a[0:15], v[8:11], v[0:3], a[0:15]
	ds_read_b128 v[0:3], v74 offset:8896
	ds_read_b128 v[8:11], v74 offset:8928
	v_mfma_f32_32x32x16_f16 a[0:15], v[12:15], v[20:23], a[0:15]
	v_mfma_f32_32x32x16_f16 a[0:15], v[32:35], v[20:23], a[0:15]
	v_mov_b32_e32 v32, v155
	v_mov_b32_e32 v34, v154
	s_waitcnt lgkmcnt(2)
	v_mfma_f32_32x32x16_f16 a[0:15], v[12:15], v[4:7], a[0:15]
	ds_read_b128 v[12:15], v40 offset:8896
	ds_read_b128 v[20:23], v40 offset:8928
	s_waitcnt lgkmcnt(0)
	s_barrier
	v_mfma_f32_32x32x16_f16 a[0:15], v[36:39], v[0:3], a[0:15]
	v_mfma_f32_32x32x16_f16 a[0:15], v[24:27], v[0:3], a[0:15]
	v_mov_b32_e32 v26, v148
	v_mov_b32_e32 v24, v149
	v_mfma_f32_32x32x16_f16 a[0:15], v[36:39], v[12:15], a[0:15]
	v_mov_b32_e32 v38, v152
	v_mov_b32_e32 v36, v153
	v_mfma_f32_32x32x16_f16 a[16:31], v[28:31], v[46:49], a[16:31]
	v_mfma_f32_32x32x16_f16 a[0:15], v[28:31], v[8:11], a[0:15]
	v_mfma_f32_32x32x16_f16 a[16:31], v[16:19], v[46:49], a[16:31]
	v_mov_b32_e32 v48, v156
	v_mov_b32_e32 v46, v157
	v_mfma_f32_32x32x16_f16 a[0:15], v[16:19], v[8:11], a[0:15]
	v_mfma_f32_32x32x16_f16 a[16:31], v[28:31], v[50:53], a[16:31]
	v_mul_f32_e32 v50, 0x43800000, v140
	v_mul_f32_e32 v51, 0x43800000, v136
	v_mul_f32_e32 v52, 0x43800000, v137
	v_mul_f32_e32 v53, 0x43800000, v138
	v_mfma_f32_32x32x16_f16 a[0:15], v[28:31], v[20:23], a[0:15]
	s_nop 6
	v_accvgpr_read_b32 v45, a18
	v_accvgpr_read_b32 v47, a17
	v_accvgpr_read_b32 v49, a16
	v_mul_f32_e64 v8, v48, s0
	v_mul_f32_e64 v9, v49, s1
	v_pk_mul_f32 v[10:11], v[46:47], s[0:1]
	v_pk_mul_f32 v[16:17], v[44:45], s[0:1]
	v_add_f32_e32 v0, v8, v9
	v_accvgpr_read_b32 v43, a19
	v_accvgpr_read_b32 v2, a0
	v_accvgpr_read_b32 v4, a1
	v_accvgpr_read_b32 v6, a2
	v_fmac_f32_e32 v8, 0x3b800000, v2
	v_add_f32_e32 v2, v10, v11
	v_fmac_f32_e32 v10, 0x3b800000, v4
	v_add_f32_e32 v4, v16, v17
	v_fmac_f32_e32 v16, 0x3b800000, v6
	v_cvt_pk_f16_f32 v20, v0, v2
	v_pk_mul_f32 v[18:19], v[42:43], s[0:1]
	v_cvt_f32_f16_e32 v6, v20
	v_cvt_f32_f16_sdwa v9, v20 dst_sel:DWORD dst_unused:UNUSED_PAD src0_sel:WORD_1
	v_add_f32_e32 v11, v18, v19
	v_cvt_pk_f16_f32 v21, v4, v11
	v_sub_f32_e32 v0, v0, v6
	v_cvt_f32_f16_e32 v6, v21
	v_sub_f32_e32 v2, v2, v9
	v_cvt_f32_f16_sdwa v9, v21 dst_sel:DWORD dst_unused:UNUSED_PAD src0_sel:WORD_1
	v_cvt_pk_f16_f32 v22, v0, v2
	v_accvgpr_read_b32 v2, a3
	v_sub_f32_e32 v4, v4, v6
	v_cvt_pk_f16_f32 v28, v8, v10
	v_fmac_f32_e32 v18, 0x3b800000, v2
	v_cvt_f32_f16_e32 v0, v28
	v_cvt_f32_f16_sdwa v2, v28 dst_sel:DWORD dst_unused:UNUSED_PAD src0_sel:WORD_1
	v_sub_f32_e32 v6, v11, v9
	v_cvt_pk_f16_f32 v23, v4, v6
	v_cvt_pk_f16_f32 v29, v16, v18
	v_accvgpr_read_b32 v37, a21
	v_cvt_f32_f16_e32 v4, v29
	v_accvgpr_read_b32 v39, a20
	v_sub_f32_e32 v0, v8, v0
	v_cvt_f32_f16_sdwa v6, v29 dst_sel:DWORD dst_unused:UNUSED_PAD src0_sel:WORD_1
	v_sub_f32_e32 v2, v10, v2
	v_accvgpr_read_b32 v33, a23
	v_sub_f32_e32 v4, v16, v4
	v_cvt_pk_f16_f32 v8, v0, v2
	v_lshlrev_b32_e32 v0, 1, v142
	v_pk_mul_f32 v[10:11], v[38:39], s[0:1]
	v_accvgpr_read_b32 v2, a4
	v_pk_mul_f32 v[16:17], v[36:37], s[0:1]
	v_lshl_or_b32 v72, v141, 3, v0
	v_add_f32_e32 v0, v10, v11
	v_fmac_f32_e32 v10, 0x3b800000, v2
	v_add_f32_e32 v2, v16, v17
	v_pk_mul_f32 v[30:31], v[32:33], s[0:1]
	v_cvt_pk_f16_f32 v32, v0, v2
	v_accvgpr_read_b32 v35, a22
	v_cvt_f32_f16_e32 v11, v32
	v_sub_f32_e32 v6, v18, v6
	v_cvt_pk_f16_f32 v9, v4, v6
	v_accvgpr_read_b32 v4, a5
	v_pk_mul_f32 v[18:19], v[34:35], s[0:1]
	v_accvgpr_read_b32 v6, a6
	v_accvgpr_read_b32 v12, a7
	v_fmac_f32_e32 v16, 0x3b800000, v4
	v_add_f32_e32 v4, v18, v19
	v_fmac_f32_e32 v18, 0x3b800000, v6
	v_add_f32_e32 v6, v30, v31
	v_fmac_f32_e32 v30, 0x3b800000, v12
	v_cvt_pk_f16_f32 v33, v4, v6
	v_sub_f32_e32 v0, v0, v11
	v_cvt_f32_f16_sdwa v11, v32 dst_sel:DWORD dst_unused:UNUSED_PAD src0_sel:WORD_1
	v_cvt_f32_f16_e32 v12, v33
	v_cvt_f32_f16_sdwa v14, v33 dst_sel:DWORD dst_unused:UNUSED_PAD src0_sel:WORD_1
	v_cvt_pk_f16_f32 v34, v10, v16
	v_sub_f32_e32 v2, v2, v11
	v_sub_f32_e32 v4, v4, v12
	v_sub_f32_e32 v6, v6, v14
	v_cvt_f32_f16_e32 v11, v34
	v_cvt_pk_f16_f32 v36, v0, v2
	v_cvt_pk_f16_f32 v37, v4, v6
	v_cvt_pk_f16_f32 v35, v18, v30
	v_cvt_f32_f16_sdwa v2, v34 dst_sel:DWORD dst_unused:UNUSED_PAD src0_sel:WORD_1
	v_cvt_f32_f16_e32 v4, v35
	v_cvt_f32_f16_sdwa v6, v35 dst_sel:DWORD dst_unused:UNUSED_PAD src0_sel:WORD_1
	v_mad_u32_u24 v31, v76, s4, v72
	v_add_u32_e32 v38, v41, v72
	v_accvgpr_read_b32 v13, a27
	v_accvgpr_read_b32 v15, a26
	v_accvgpr_read_b32 v25, a25
	v_accvgpr_read_b32 v27, a24
	v_sub_f32_e32 v0, v10, v11
	v_sub_f32_e32 v2, v16, v2
	v_sub_f32_e32 v4, v18, v4
	v_sub_f32_e32 v6, v30, v6
	v_cvt_pk_f16_f32 v10, v0, v2
	v_cvt_pk_f16_f32 v11, v4, v6
	ds_write2_b64 v31, v[20:21], v[32:33] offset1:2
	ds_write2_b64 v38, v[22:23], v[36:37] offset1:2
	v_add_u32_e32 v23, 0x2000, v38
	v_mov_b32_e32 v14, v150
	v_mov_b32_e32 v12, v151
	ds_write2_b64 v23, v[8:9], v[10:11] offset0:64 offset1:66
	v_pk_mul_f32 v[8:9], v[26:27], s[0:1]
	v_accvgpr_read_b32 v2, a8
	v_pk_mul_f32 v[10:11], v[24:25], s[0:1]
	v_accvgpr_read_b32 v4, a9
	v_pk_mul_f32 v[14:15], v[14:15], s[0:1]
	v_accvgpr_read_b32 v6, a10
	v_pk_mul_f32 v[12:13], v[12:13], s[0:1]
	v_add_f32_e32 v0, v8, v9
	v_fmac_f32_e32 v8, 0x3b800000, v2
	v_add_f32_e32 v2, v10, v11
	v_fmac_f32_e32 v10, 0x3b800000, v4
	v_add_f32_e32 v4, v14, v15
	v_fmac_f32_e32 v14, 0x3b800000, v6
	v_add_f32_e32 v6, v12, v13
	v_accvgpr_read_b32 v9, a11
	v_cvt_pk_f16_f32 v17, v4, v6
	v_fmac_f32_e32 v12, 0x3b800000, v9
	v_cvt_f32_f16_sdwa v15, v17 dst_sel:DWORD dst_unused:UNUSED_PAD src0_sel:WORD_1
	v_cvt_pk_f16_f32 v16, v0, v2
	v_cvt_f32_f16_e32 v13, v17
	v_cvt_f32_f16_e32 v9, v16
	v_cvt_f32_f16_sdwa v11, v16 dst_sel:DWORD dst_unused:UNUSED_PAD src0_sel:WORD_1
	v_sub_f32_e32 v6, v6, v15
	v_sub_f32_e32 v4, v4, v13
	v_sub_f32_e32 v0, v0, v9
	v_cvt_pk_f16_f32 v19, v4, v6
	v_cvt_pk_f16_f32 v21, v14, v12
	v_sub_f32_e32 v2, v2, v11
	v_cvt_f32_f16_sdwa v6, v21 dst_sel:DWORD dst_unused:UNUSED_PAD src0_sel:WORD_1
	v_cvt_pk_f16_f32 v18, v0, v2
	v_cvt_pk_f16_f32 v20, v8, v10
	v_cvt_f32_f16_e32 v4, v21
	v_cvt_f32_f16_e32 v0, v20
	v_cvt_f32_f16_sdwa v2, v20 dst_sel:DWORD dst_unused:UNUSED_PAD src0_sel:WORD_1
	v_sub_f32_e32 v6, v12, v6
	v_accvgpr_read_b32 v7, a28
	v_sub_f32_e32 v0, v8, v0
	v_sub_f32_e32 v4, v14, v4
	v_cvt_pk_f16_f32 v9, v4, v6
	v_mov_b32_e32 v6, v144
	v_accvgpr_read_b32 v5, a29
	v_sub_f32_e32 v2, v10, v2
	v_cvt_pk_f16_f32 v8, v0, v2
	v_pk_mul_f32 v[6:7], v[6:7], s[0:1]
	v_accvgpr_read_b32 v0, a12
	v_mov_b32_e32 v4, v145
	v_accvgpr_read_b32 v3, a30
	v_add_f32_e32 v7, v6, v7
	v_fmac_f32_e32 v6, 0x3b800000, v0
	v_pk_mul_f32 v[4:5], v[4:5], s[0:1]
	v_accvgpr_read_b32 v0, a13
	v_mov_b32_e32 v2, v146
	v_add_f32_e32 v5, v4, v5
	v_fmac_f32_e32 v4, 0x3b800000, v0
	v_pk_mul_f32 v[2:3], v[2:3], s[0:1]
	v_accvgpr_read_b32 v0, a14
	v_accvgpr_read_b32 v1, a31
	v_add_f32_e32 v3, v2, v3
	v_fmac_f32_e32 v2, 0x3b800000, v0
	v_mov_b32_e32 v0, v147
	v_pk_mul_f32 v[0:1], v[0:1], s[0:1]
	v_accvgpr_read_b32 v10, a15
	v_add_f32_e32 v1, v0, v1
	v_cvt_pk_f16_f32 v11, v3, v1
	v_fmac_f32_e32 v0, 0x3b800000, v10
	v_cvt_f32_f16_sdwa v15, v11 dst_sel:DWORD dst_unused:UNUSED_PAD src0_sel:WORD_1
	v_cvt_pk_f16_f32 v10, v7, v5
	v_cvt_f32_f16_e32 v14, v11
	v_cvt_f32_f16_e32 v12, v10
	v_cvt_f32_f16_sdwa v13, v10 dst_sel:DWORD dst_unused:UNUSED_PAD src0_sel:WORD_1
	v_sub_f32_e32 v1, v1, v15
	v_sub_f32_e32 v3, v3, v14
	v_sub_f32_e32 v7, v7, v12
	v_sub_f32_e32 v5, v5, v13
	v_cvt_pk_f16_f32 v13, v3, v1
	v_cvt_pk_f16_f32 v14, v6, v4
	v_cvt_pk_f16_f32 v12, v7, v5
	v_cvt_pk_f16_f32 v15, v2, v0
	v_add_u32_e32 v22, 0x2000, v31
	v_cvt_f32_f16_e32 v1, v14
	v_cvt_f32_f16_sdwa v3, v14 dst_sel:DWORD dst_unused:UNUSED_PAD src0_sel:WORD_1
	v_cvt_f32_f16_e32 v5, v15
	v_cvt_f32_f16_sdwa v7, v15 dst_sel:DWORD dst_unused:UNUSED_PAD src0_sel:WORD_1
	v_sub_f32_e32 v1, v6, v1
	v_sub_f32_e32 v3, v4, v3
	v_sub_f32_e32 v2, v2, v5
	v_sub_f32_e32 v4, v0, v7
	v_cvt_pk_f16_f32 v0, v1, v3
	v_cvt_pk_f16_f32 v1, v2, v4
	ds_write2_b64 v22, v[28:29], v[34:35] offset0:64 offset1:66
	ds_write2_b64 v31, v[16:17], v[10:11] offset0:4 offset1:6
	ds_write2_b64 v38, v[18:19], v[12:13] offset0:4 offset1:6
	ds_write2_b64 v22, v[20:21], v[14:15] offset0:68 offset1:70
	ds_write2_b64 v23, v[8:9], v[0:1] offset0:68 offset1:70
	s_waitcnt lgkmcnt(0)
	s_barrier
	ds_read_b128 v[0:3], v74
	ds_read_b128 v[8:11], v74 offset:32
	ds_read_b128 v[12:15], v74 offset:8704
	ds_read_b128 v[16:19], v74 offset:8736
	v_cvt_pk_f16_f32 v4, v50, v51
	v_cvt_pk_f16_f32 v5, v52, v53
	v_cvt_pk_f16_f32 v6, v54, v55
	v_cvt_pk_f16_f32 v7, v56, v57
	v_mul_f32_e32 v28, 0x43800000, v124
	s_waitcnt lgkmcnt(3)
	v_mfma_f32_32x32x16_f16 a[0:15], v[4:7], v[0:3], 0
	v_fma_mix_f32 v20, v140, s3, -v4 op_sel_hi:[0,0,1]
	v_fma_mix_f32 v21, v136, s3, -v4 op_sel:[0,0,1] op_sel_hi:[0,0,1]
	v_fma_mix_f32 v22, v137, s3, -v5 op_sel_hi:[0,0,1]
	v_fma_mix_f32 v23, v138, s3, -v5 op_sel:[0,0,1] op_sel_hi:[0,0,1]
	v_fma_mix_f32 v24, v139, s3, -v6 op_sel_hi:[0,0,1]
	v_fma_mix_f32 v25, v133, s3, -v6 op_sel:[0,0,1] op_sel_hi:[0,0,1]
	v_fma_mix_f32 v26, v134, s3, -v7 op_sel_hi:[0,0,1]
	s_waitcnt lgkmcnt(1)
	v_mfma_f32_32x32x16_f16 a[16:31], v[4:7], v[12:15], 0
	v_fma_mix_f32 v27, v135, s3, -v7 op_sel:[0,0,1] op_sel_hi:[0,0,1]
	v_cvt_pk_f16_f32 v20, v20, v21
	v_cvt_pk_f16_f32 v21, v22, v23
	v_cvt_pk_f16_f32 v22, v24, v25
	v_cvt_pk_f16_f32 v23, v26, v27
	v_mul_f32_e32 v24, 0x43800000, v120
	v_mul_f32_e32 v25, 0x43800000, v121
	v_mfma_f32_32x32x16_f16 a[0:15], v[20:23], v[0:3], a[0:15]
	v_mul_f32_e32 v26, 0x43800000, v122
	v_mul_f32_e32 v27, 0x43800000, v123
	s_mov_b64 s[0:1], 0x2000
	v_mfma_f32_32x32x16_f16 a[16:31], v[20:23], v[12:15], a[16:31]
	ds_read_b128 v[0:3], v40
	ds_read_b128 v[12:15], v40 offset:32
	ds_read_b128 v[20:23], v40 offset:8736
	s_waitcnt lgkmcnt(2)
	v_mfma_f32_32x32x16_f16 a[0:15], v[4:7], v[0:3], a[0:15]
	ds_read_b128 v[0:3], v40 offset:8704
	s_waitcnt lgkmcnt(0)
	v_mfma_f32_32x32x16_f16 a[16:31], v[4:7], v[0:3], a[16:31]
	v_mul_f32_e32 v2, 0x43800000, v117
	v_mul_f32_e32 v3, 0x43800000, v118
	v_mul_f32_e32 v4, 0x43800000, v119
	v_cvt_pk_f16_f32 v0, v24, v25
	v_cvt_pk_f16_f32 v1, v26, v27
	v_cvt_pk_f16_f32 v2, v28, v2
	v_cvt_pk_f16_f32 v3, v3, v4
	v_mul_f32_e32 v28, 0x43800000, v116
	v_mfma_f32_32x32x16_f16 a[0:15], v[0:3], v[8:11], a[0:15]
	v_fma_mix_f32 v4, v120, s3, -v0 op_sel_hi:[0,0,1]
	v_fma_mix_f32 v5, v121, s3, -v0 op_sel:[0,0,1] op_sel_hi:[0,0,1]
	v_fma_mix_f32 v6, v122, s3, -v1 op_sel_hi:[0,0,1]
	v_fma_mix_f32 v7, v123, s3, -v1 op_sel:[0,0,1] op_sel_hi:[0,0,1]
	v_fma_mix_f32 v24, v124, s3, -v2 op_sel_hi:[0,0,1]
	v_fma_mix_f32 v25, v117, s3, -v2 op_sel:[0,0,1] op_sel_hi:[0,0,1]
	v_fma_mix_f32 v26, v118, s3, -v3 op_sel_hi:[0,0,1]
	v_mfma_f32_32x32x16_f16 a[16:31], v[0:3], v[16:19], a[16:31]
	v_fma_mix_f32 v27, v119, s3, -v3 op_sel:[0,0,1] op_sel_hi:[0,0,1]
	v_cvt_pk_f16_f32 v4, v4, v5
	v_cvt_pk_f16_f32 v5, v6, v7
	v_cvt_pk_f16_f32 v6, v24, v25
	v_cvt_pk_f16_f32 v7, v26, v27
	s_nop 0
	v_mfma_f32_32x32x16_f16 a[0:15], v[4:7], v[8:11], a[0:15]
	v_mul_f32_e32 v8, 0x43800000, v131
	v_mul_f32_e32 v9, 0x43800000, v125
	v_mul_f32_e32 v10, 0x43800000, v126
	v_mul_f32_e32 v11, 0x43800000, v127
	v_mfma_f32_32x32x16_f16 a[16:31], v[4:7], v[16:19], a[16:31]
	v_mul_f32_e32 v4, 0x43800000, v132
	v_mul_f32_e32 v5, 0x43800000, v128
	v_mul_f32_e32 v6, 0x43800000, v129
	v_mul_f32_e32 v7, 0x43800000, v130
	v_cvt_pk_f16_f32 v4, v4, v5
	v_cvt_pk_f16_f32 v5, v6, v7
	v_cvt_pk_f16_f32 v6, v8, v9
	v_mfma_f32_32x32x16_f16 a[0:15], v[0:3], v[12:15], a[0:15]
	ds_read_b128 v[12:15], v74 offset:8768
	ds_read_b128 v[16:19], v74 offset:8800
	v_cvt_pk_f16_f32 v7, v10, v11
	ds_read_b128 v[8:11], v74 offset:96
	v_fma_mix_f32 v24, v131, s3, -v6 op_sel_hi:[0,0,1]
	v_fma_mix_f32 v25, v125, s3, -v6 op_sel:[0,0,1] op_sel_hi:[0,0,1]
	v_fma_mix_f32 v26, v126, s3, -v7 op_sel_hi:[0,0,1]
	v_mfma_f32_32x32x16_f16 a[16:31], v[0:3], v[20:23], a[16:31]
	ds_read_b128 v[0:3], v74 offset:64
	v_fma_mix_f32 v20, v132, s3, -v4 op_sel_hi:[0,0,1]
	v_fma_mix_f32 v21, v128, s3, -v4 op_sel:[0,0,1] op_sel_hi:[0,0,1]
	v_fma_mix_f32 v22, v129, s3, -v5 op_sel_hi:[0,0,1]
	v_fma_mix_f32 v23, v130, s3, -v5 op_sel:[0,0,1] op_sel_hi:[0,0,1]
	v_fma_mix_f32 v27, v127, s3, -v7 op_sel:[0,0,1] op_sel_hi:[0,0,1]
	v_cvt_pk_f16_f32 v20, v20, v21
	s_waitcnt lgkmcnt(0)
	v_mfma_f32_32x32x16_f16 a[0:15], v[4:7], v[0:3], a[0:15]
	v_cvt_pk_f16_f32 v21, v22, v23
	v_cvt_pk_f16_f32 v22, v24, v25
	v_cvt_pk_f16_f32 v23, v26, v27
	v_mul_f32_e32 v24, 0x43800000, v112
	v_mul_f32_e32 v25, 0x43800000, v113
	v_mul_f32_e32 v26, 0x43800000, v114
	v_mul_f32_e32 v27, 0x43800000, v115
	v_mfma_f32_32x32x16_f16 a[16:31], v[4:7], v[12:15], a[16:31]
	v_mfma_f32_32x32x16_f16 a[0:15], v[20:23], v[0:3], a[0:15]
	v_mfma_f32_32x32x16_f16 a[16:31], v[20:23], v[12:15], a[16:31]
	ds_read_b128 v[0:3], v40 offset:64
	ds_read_b128 v[12:15], v40 offset:96
	ds_read_b128 v[20:23], v40 offset:8800
	s_waitcnt lgkmcnt(2)
	v_mfma_f32_32x32x16_f16 a[0:15], v[4:7], v[0:3], a[0:15]
	ds_read_b128 v[0:3], v40 offset:8768
	s_waitcnt lgkmcnt(0)
	v_mfma_f32_32x32x16_f16 a[16:31], v[4:7], v[0:3], a[16:31]
	v_mul_f32_e32 v2, 0x43800000, v109
	v_mul_f32_e32 v3, 0x43800000, v110
	v_mul_f32_e32 v4, 0x43800000, v111
	v_cvt_pk_f16_f32 v0, v24, v25
	v_cvt_pk_f16_f32 v1, v26, v27
	v_cvt_pk_f16_f32 v2, v28, v2
	v_cvt_pk_f16_f32 v3, v3, v4
	v_mul_f32_e32 v28, 0x43800000, v95
	v_mfma_f32_32x32x16_f16 a[0:15], v[0:3], v[8:11], a[0:15]
	v_fma_mix_f32 v4, v112, s3, -v0 op_sel_hi:[0,0,1]
	v_fma_mix_f32 v5, v113, s3, -v0 op_sel:[0,0,1] op_sel_hi:[0,0,1]
	v_fma_mix_f32 v6, v114, s3, -v1 op_sel_hi:[0,0,1]
	v_fma_mix_f32 v7, v115, s3, -v1 op_sel:[0,0,1] op_sel_hi:[0,0,1]
	v_fma_mix_f32 v24, v116, s3, -v2 op_sel_hi:[0,0,1]
	v_fma_mix_f32 v25, v109, s3, -v2 op_sel:[0,0,1] op_sel_hi:[0,0,1]
	v_fma_mix_f32 v26, v110, s3, -v3 op_sel_hi:[0,0,1]
	v_mfma_f32_32x32x16_f16 a[16:31], v[0:3], v[16:19], a[16:31]
	v_fma_mix_f32 v27, v111, s3, -v3 op_sel:[0,0,1] op_sel_hi:[0,0,1]
	v_cvt_pk_f16_f32 v4, v4, v5
	v_cvt_pk_f16_f32 v5, v6, v7
	v_cvt_pk_f16_f32 v6, v24, v25
	v_cvt_pk_f16_f32 v7, v26, v27
	s_nop 0
	v_mfma_f32_32x32x16_f16 a[0:15], v[4:7], v[8:11], a[0:15]
	v_mul_f32_e32 v8, 0x43800000, v107
	v_mul_f32_e32 v9, 0x43800000, v101
	v_mul_f32_e32 v10, 0x43800000, v102
	v_mul_f32_e32 v11, 0x43800000, v103
	v_mfma_f32_32x32x16_f16 a[16:31], v[4:7], v[16:19], a[16:31]
	v_mul_f32_e32 v4, 0x43800000, v108
	v_mul_f32_e32 v5, 0x43800000, v104
	v_mul_f32_e32 v6, 0x43800000, v105
	v_mul_f32_e32 v7, 0x43800000, v106
	v_cvt_pk_f16_f32 v4, v4, v5
	v_cvt_pk_f16_f32 v5, v6, v7
	v_cvt_pk_f16_f32 v6, v8, v9
	v_mfma_f32_32x32x16_f16 a[0:15], v[0:3], v[12:15], a[0:15]
	ds_read_b128 v[12:15], v74 offset:8832
	ds_read_b128 v[16:19], v74 offset:8864
	v_cvt_pk_f16_f32 v7, v10, v11
	ds_read_b128 v[8:11], v74 offset:160
	v_fma_mix_f32 v24, v107, s3, -v6 op_sel_hi:[0,0,1]
	v_fma_mix_f32 v25, v101, s3, -v6 op_sel:[0,0,1] op_sel_hi:[0,0,1]
	v_fma_mix_f32 v26, v102, s3, -v7 op_sel_hi:[0,0,1]
	v_mfma_f32_32x32x16_f16 a[16:31], v[0:3], v[20:23], a[16:31]
	ds_read_b128 v[0:3], v74 offset:128
	v_fma_mix_f32 v20, v108, s3, -v4 op_sel_hi:[0,0,1]
	v_fma_mix_f32 v21, v104, s3, -v4 op_sel:[0,0,1] op_sel_hi:[0,0,1]
	v_fma_mix_f32 v22, v105, s3, -v5 op_sel_hi:[0,0,1]
	v_fma_mix_f32 v23, v106, s3, -v5 op_sel:[0,0,1] op_sel_hi:[0,0,1]
	v_fma_mix_f32 v27, v103, s3, -v7 op_sel:[0,0,1] op_sel_hi:[0,0,1]
	v_cvt_pk_f16_f32 v20, v20, v21
	s_waitcnt lgkmcnt(0)
	v_mfma_f32_32x32x16_f16 a[0:15], v[4:7], v[0:3], a[0:15]
	v_cvt_pk_f16_f32 v21, v22, v23
	v_cvt_pk_f16_f32 v22, v24, v25
	v_cvt_pk_f16_f32 v23, v26, v27
	v_mul_f32_e32 v24, 0x43800000, v91
	v_mul_f32_e32 v25, 0x43800000, v92
	v_mul_f32_e32 v26, 0x43800000, v93
	v_mul_f32_e32 v27, 0x43800000, v94
	v_mfma_f32_32x32x16_f16 a[16:31], v[4:7], v[12:15], a[16:31]
	v_mfma_f32_32x32x16_f16 a[0:15], v[20:23], v[0:3], a[0:15]
	v_mfma_f32_32x32x16_f16 a[16:31], v[20:23], v[12:15], a[16:31]
	ds_read_b128 v[0:3], v40 offset:128
	ds_read_b128 v[12:15], v40 offset:160
	ds_read_b128 v[20:23], v40 offset:8864
	s_waitcnt lgkmcnt(2)
	v_mfma_f32_32x32x16_f16 a[0:15], v[4:7], v[0:3], a[0:15]
	ds_read_b128 v[0:3], v40 offset:8832
	s_waitcnt lgkmcnt(0)
	v_mfma_f32_32x32x16_f16 a[16:31], v[4:7], v[0:3], a[16:31]
	v_mul_f32_e32 v2, 0x43800000, v88
	v_mul_f32_e32 v3, 0x43800000, v89
	v_mul_f32_e32 v4, 0x43800000, v90
	v_cvt_pk_f16_f32 v0, v24, v25
	v_cvt_pk_f16_f32 v1, v26, v27
	v_cvt_pk_f16_f32 v2, v28, v2
	v_cvt_pk_f16_f32 v3, v3, v4
	v_mul_f32_e32 v28, 0x43800000, v84
	v_mfma_f32_32x32x16_f16 a[0:15], v[0:3], v[8:11], a[0:15]
	v_fma_mix_f32 v4, v91, s3, -v0 op_sel_hi:[0,0,1]
	v_fma_mix_f32 v5, v92, s3, -v0 op_sel:[0,0,1] op_sel_hi:[0,0,1]
	v_fma_mix_f32 v6, v93, s3, -v1 op_sel_hi:[0,0,1]
	v_fma_mix_f32 v7, v94, s3, -v1 op_sel:[0,0,1] op_sel_hi:[0,0,1]
	v_fma_mix_f32 v24, v95, s3, -v2 op_sel_hi:[0,0,1]
	v_fma_mix_f32 v25, v88, s3, -v2 op_sel:[0,0,1] op_sel_hi:[0,0,1]
	v_fma_mix_f32 v26, v89, s3, -v3 op_sel_hi:[0,0,1]
	v_mfma_f32_32x32x16_f16 a[16:31], v[0:3], v[16:19], a[16:31]
	v_fma_mix_f32 v27, v90, s3, -v3 op_sel:[0,0,1] op_sel_hi:[0,0,1]
	v_cvt_pk_f16_f32 v4, v4, v5
	v_cvt_pk_f16_f32 v5, v6, v7
	v_cvt_pk_f16_f32 v6, v24, v25
	v_cvt_pk_f16_f32 v7, v26, v27
	s_nop 0
	v_mfma_f32_32x32x16_f16 a[0:15], v[4:7], v[8:11], a[0:15]
	v_mul_f32_e32 v8, 0x43800000, v99
	v_mul_f32_e32 v9, 0x43800000, v85
	v_mul_f32_e32 v10, 0x43800000, v86
	v_mul_f32_e32 v11, 0x43800000, v87
	v_mfma_f32_32x32x16_f16 a[16:31], v[4:7], v[16:19], a[16:31]
	v_mul_f32_e32 v4, 0x43800000, v100
	v_mul_f32_e32 v5, 0x43800000, v96
	v_mul_f32_e32 v6, 0x43800000, v97
	v_mul_f32_e32 v7, 0x43800000, v98
	v_cvt_pk_f16_f32 v4, v4, v5
	v_cvt_pk_f16_f32 v5, v6, v7
	v_cvt_pk_f16_f32 v6, v8, v9
	v_mfma_f32_32x32x16_f16 a[0:15], v[0:3], v[12:15], a[0:15]
	ds_read_b128 v[12:15], v74 offset:8896
	ds_read_b128 v[16:19], v74 offset:8928
	v_cvt_pk_f16_f32 v7, v10, v11
	ds_read_b128 v[8:11], v74 offset:224
	v_fma_mix_f32 v24, v99, s3, -v6 op_sel_hi:[0,0,1]
	v_fma_mix_f32 v25, v85, s3, -v6 op_sel:[0,0,1] op_sel_hi:[0,0,1]
	v_fma_mix_f32 v26, v86, s3, -v7 op_sel_hi:[0,0,1]
	v_mfma_f32_32x32x16_f16 a[16:31], v[0:3], v[20:23], a[16:31]
	ds_read_b128 v[0:3], v74 offset:192
	v_fma_mix_f32 v20, v100, s3, -v4 op_sel_hi:[0,0,1]
	v_fma_mix_f32 v21, v96, s3, -v4 op_sel:[0,0,1] op_sel_hi:[0,0,1]
	v_fma_mix_f32 v22, v97, s3, -v5 op_sel_hi:[0,0,1]
	v_fma_mix_f32 v23, v98, s3, -v5 op_sel:[0,0,1] op_sel_hi:[0,0,1]
	v_fma_mix_f32 v27, v87, s3, -v7 op_sel:[0,0,1] op_sel_hi:[0,0,1]
	v_cvt_pk_f16_f32 v20, v20, v21
	s_waitcnt lgkmcnt(0)
	v_mfma_f32_32x32x16_f16 a[0:15], v[4:7], v[0:3], a[0:15]
	v_cvt_pk_f16_f32 v21, v22, v23
	v_cvt_pk_f16_f32 v22, v24, v25
	v_cvt_pk_f16_f32 v23, v26, v27
	v_mul_f32_e32 v24, 0x43800000, v80
	v_mul_f32_e32 v25, 0x43800000, v81
	v_mul_f32_e32 v26, 0x43800000, v82
	v_mul_f32_e32 v27, 0x43800000, v83
	v_mfma_f32_32x32x16_f16 a[16:31], v[4:7], v[12:15], a[16:31]
	v_or_b32_e32 v74, s2, v76
	v_mfma_f32_32x32x16_f16 a[0:15], v[20:23], v[0:3], a[0:15]
	v_mfma_f32_32x32x16_f16 a[16:31], v[20:23], v[12:15], a[16:31]
	ds_read_b128 v[0:3], v40 offset:192
	ds_read_b128 v[12:15], v40 offset:224
	ds_read_b128 v[20:23], v40 offset:8928
	s_waitcnt lgkmcnt(2)
	v_mfma_f32_32x32x16_f16 a[0:15], v[4:7], v[0:3], a[0:15]
	ds_read_b128 v[0:3], v40 offset:8896
	s_waitcnt lgkmcnt(0)
	v_mfma_f32_32x32x16_f16 a[16:31], v[4:7], v[0:3], a[16:31]
	v_mul_f32_e32 v2, 0x43800000, v77
	v_mul_f32_e32 v3, 0x43800000, v78
	v_mul_f32_e32 v4, 0x43800000, v79
	v_cvt_pk_f16_f32 v0, v24, v25
	v_cvt_pk_f16_f32 v1, v26, v27
	v_cvt_pk_f16_f32 v2, v28, v2
	v_cvt_pk_f16_f32 v3, v3, v4
	s_nop 0
	v_mfma_f32_32x32x16_f16 a[0:15], v[0:3], v[8:11], a[0:15]
	v_fma_mix_f32 v4, v80, s3, -v0 op_sel_hi:[0,0,1]
	v_fma_mix_f32 v5, v81, s3, -v0 op_sel:[0,0,1] op_sel_hi:[0,0,1]
	v_fma_mix_f32 v6, v82, s3, -v1 op_sel_hi:[0,0,1]
	v_fma_mix_f32 v7, v83, s3, -v1 op_sel:[0,0,1] op_sel_hi:[0,0,1]
	v_fma_mix_f32 v24, v84, s3, -v2 op_sel_hi:[0,0,1]
	v_fma_mix_f32 v25, v77, s3, -v2 op_sel:[0,0,1] op_sel_hi:[0,0,1]
	v_fma_mix_f32 v26, v78, s3, -v3 op_sel_hi:[0,0,1]
	v_mfma_f32_32x32x16_f16 a[16:31], v[0:3], v[16:19], a[16:31]
	v_fma_mix_f32 v27, v79, s3, -v3 op_sel:[0,0,1] op_sel_hi:[0,0,1]
	v_cvt_pk_f16_f32 v4, v4, v5
	v_cvt_pk_f16_f32 v5, v6, v7
	v_cvt_pk_f16_f32 v6, v24, v25
	v_cvt_pk_f16_f32 v7, v26, v27
	s_nop 0
	v_mfma_f32_32x32x16_f16 a[0:15], v[4:7], v[8:11], a[0:15]
	v_mfma_f32_32x32x16_f16 a[16:31], v[4:7], v[16:19], a[16:31]
	v_mfma_f32_32x32x16_f16 a[0:15], v[0:3], v[12:15], a[0:15]
	v_mfma_f32_32x32x16_f16 a[16:31], v[0:3], v[20:23], a[16:31]
	s_nop 15
	v_and_b32_e32 v10, 31, v187
	v_bfe_u32 v11, v187, 5, 1
	v_lshrrev_b32_e32 v12, 6, v187
	v_and_b32_e32 v13, 63, v187
	v_lshrrev_b32_e32 v14, 2, v13
	v_and_b32_e32 v15, 3, v13
	v_and_b32_e32 v16, 3, v10
	v_lshlrev_b32_e32 v16, 4, v16
	v_lshlrev_b32_e32 v17, 6, v10
	v_lshl_add_u32 v17, v11, 3, v17
	v_lshl_add_u32 v17, v12, 12, v17
	v_add_u32_e32 v17, 0x8800, v17
	v_and_b32_e32 v18, 3, v14
	v_xor_b32_e32 v18, v18, v15
	v_lshlrev_b32_e32 v18, 4, v18
	v_lshl_add_u32 v18, v14, 6, v18
	v_lshl_add_u32 v18, v12, 12, v18
	v_add_u32_e32 v18, 0x8800, v18
	v_add_u32_e32 v22, s2, v14
	v_mov_b32_e32 v23, 0
	v_lshlrev_b64 v[22:23], 8, v[22:23]
	v_lshl_add_u64 v[22:23], v[22:23], 0, s[12:13]
	v_lshlrev_b32_e32 v24, 6, v12
	v_lshl_add_u32 v24, v15, 4, v24
	v_mov_b32_e32 v25, 0
	v_lshl_add_u64 v[22:23], v[22:23], 0, v[24:25]
	s_mov_b64 s[28:29], 0x1000
	v_lshl_add_u64 v[24:25], v[22:23], 0, s[28:29]
	v_lshl_add_u64 v[26:27], v[24:25], 0, s[28:29]
	v_lshl_add_u64 v[28:29], v[26:27], 0, s[28:29]
	v_accvgpr_read_b32 v44, a0
	v_accvgpr_read_b32 v45, a1
	v_accvgpr_read_b32 v46, a2
	v_accvgpr_read_b32 v47, a3
	v_mul_f32_e32 v44, 0x39b8aa3b, v44
	v_mul_f32_e32 v45, 0x39b8aa3b, v45
	v_mul_f32_e32 v46, 0x39b8aa3b, v46
	v_mul_f32_e32 v47, 0x39b8aa3b, v47
	v_cvt_pk_f16_f32 v44, v44, v45
	v_cvt_pk_f16_f32 v45, v46, v47
	v_xor_b32_e32 v48, 0x0, v16
	v_add_u32_e32 v48, v48, v17
	ds_write_b64 v48, v[44:45] offset:0
	v_accvgpr_read_b32 v52, a4
	v_accvgpr_read_b32 v53, a5
	v_accvgpr_read_b32 v54, a6
	v_accvgpr_read_b32 v55, a7
	v_mul_f32_e32 v52, 0x39b8aa3b, v52
	v_mul_f32_e32 v53, 0x39b8aa3b, v53
	v_mul_f32_e32 v54, 0x39b8aa3b, v54
	v_mul_f32_e32 v55, 0x39b8aa3b, v55
	v_cvt_pk_f16_f32 v52, v52, v53
	v_cvt_pk_f16_f32 v53, v54, v55
	v_xor_b32_e32 v56, 0x10, v16
	v_add_u32_e32 v56, v56, v17
	ds_write_b64 v56, v[52:53] offset:0
	v_accvgpr_read_b32 v60, a8
	v_accvgpr_read_b32 v61, a9
	v_accvgpr_read_b32 v62, a10
	v_accvgpr_read_b32 v63, a11
	v_mul_f32_e32 v60, 0x39b8aa3b, v60
	v_mul_f32_e32 v61, 0x39b8aa3b, v61
	v_mul_f32_e32 v62, 0x39b8aa3b, v62
	v_mul_f32_e32 v63, 0x39b8aa3b, v63
	v_cvt_pk_f16_f32 v60, v60, v61
	v_cvt_pk_f16_f32 v61, v62, v63
	v_xor_b32_e32 v64, 0x20, v16
	v_add_u32_e32 v64, v64, v17
	ds_write_b64 v64, v[60:61] offset:0
	v_accvgpr_read_b32 v68, a12
	v_accvgpr_read_b32 v69, a13
	v_accvgpr_read_b32 v70, a14
	v_accvgpr_read_b32 v71, a15
	v_mul_f32_e32 v68, 0x39b8aa3b, v68
	v_mul_f32_e32 v69, 0x39b8aa3b, v69
	v_mul_f32_e32 v70, 0x39b8aa3b, v70
	v_mul_f32_e32 v71, 0x39b8aa3b, v71
	v_cvt_pk_f16_f32 v68, v68, v69
	v_cvt_pk_f16_f32 v69, v70, v71
	v_xor_b32_e32 v72, 0x30, v16
	v_add_u32_e32 v72, v72, v17
	ds_write_b64 v72, v[68:69] offset:0
	v_accvgpr_read_b32 v76, a16
	v_accvgpr_read_b32 v77, a17
	v_accvgpr_read_b32 v78, a18
	v_accvgpr_read_b32 v79, a19
	v_mul_f32_e32 v76, 0x39b8aa3b, v76
	v_mul_f32_e32 v77, 0x39b8aa3b, v77
	v_mul_f32_e32 v78, 0x39b8aa3b, v78
	v_mul_f32_e32 v79, 0x39b8aa3b, v79
	v_cvt_pk_f16_f32 v76, v76, v77
	v_cvt_pk_f16_f32 v77, v78, v79
	v_xor_b32_e32 v80, 0x0, v16
	v_add_u32_e32 v80, v80, v17
	ds_write_b64 v80, v[76:77] offset:2048
	v_accvgpr_read_b32 v84, a20
	v_accvgpr_read_b32 v85, a21
	v_accvgpr_read_b32 v86, a22
	v_accvgpr_read_b32 v87, a23
	v_mul_f32_e32 v84, 0x39b8aa3b, v84
	v_mul_f32_e32 v85, 0x39b8aa3b, v85
	v_mul_f32_e32 v86, 0x39b8aa3b, v86
	v_mul_f32_e32 v87, 0x39b8aa3b, v87
	v_cvt_pk_f16_f32 v84, v84, v85
	v_cvt_pk_f16_f32 v85, v86, v87
	v_xor_b32_e32 v88, 0x10, v16
	v_add_u32_e32 v88, v88, v17
	ds_write_b64 v88, v[84:85] offset:2048
	v_accvgpr_read_b32 v92, a24
	v_accvgpr_read_b32 v93, a25
	v_accvgpr_read_b32 v94, a26
	v_accvgpr_read_b32 v95, a27
	v_mul_f32_e32 v92, 0x39b8aa3b, v92
	v_mul_f32_e32 v93, 0x39b8aa3b, v93
	v_mul_f32_e32 v94, 0x39b8aa3b, v94
	v_mul_f32_e32 v95, 0x39b8aa3b, v95
	v_cvt_pk_f16_f32 v92, v92, v93
	v_cvt_pk_f16_f32 v93, v94, v95
	v_xor_b32_e32 v96, 0x20, v16
	v_add_u32_e32 v96, v96, v17
	ds_write_b64 v96, v[92:93] offset:2048
	v_accvgpr_read_b32 v100, a28
	v_accvgpr_read_b32 v101, a29
	v_accvgpr_read_b32 v102, a30
	v_accvgpr_read_b32 v103, a31
	v_mul_f32_e32 v100, 0x39b8aa3b, v100
	v_mul_f32_e32 v101, 0x39b8aa3b, v101
	v_mul_f32_e32 v102, 0x39b8aa3b, v102
	v_mul_f32_e32 v103, 0x39b8aa3b, v103
	v_cvt_pk_f16_f32 v100, v100, v101
	v_cvt_pk_f16_f32 v101, v102, v103
	v_xor_b32_e32 v104, 0x30, v16
	v_add_u32_e32 v104, v104, v17
	ds_write_b64 v104, v[100:101] offset:2048
	s_waitcnt lgkmcnt(0)
	ds_read_b128 v[30:33], v18 offset:0
	ds_read_b128 v[34:37], v18 offset:1024
	ds_read_b128 v[38:41], v18 offset:2048
	ds_read_b128 v[42:45], v18 offset:3072
	s_waitcnt lgkmcnt(3)
	global_store_dwordx4 v[22:23], v[30:33], off sc1
	s_waitcnt lgkmcnt(2)
	global_store_dwordx4 v[24:25], v[34:37], off sc1
	s_waitcnt lgkmcnt(1)
	global_store_dwordx4 v[26:27], v[38:41], off sc1
	s_waitcnt lgkmcnt(0)
	global_store_dwordx4 v[28:29], v[42:45], off sc1
	s_endpgm

	.amdhsa_kernel _Z11prep_kernelPKfS0_S0_S0_PDF16_S1_S0_S1_
		.amdhsa_group_segment_fixed_size 51200
		.amdhsa_private_segment_fixed_size 0
		.amdhsa_kernarg_size 64
		.amdhsa_user_sgpr_count 2
		.amdhsa_user_sgpr_dispatch_ptr 0
		.amdhsa_user_sgpr_queue_ptr 0
		.amdhsa_user_sgpr_kernarg_segment_ptr 1
		.amdhsa_user_sgpr_dispatch_id 0
		.amdhsa_user_sgpr_kernarg_preload_length 0
		.amdhsa_user_sgpr_kernarg_preload_offset 0
		.amdhsa_user_sgpr_private_segment_size 0
		.amdhsa_uses_dynamic_stack 0
		.amdhsa_enable_private_segment 0
		.amdhsa_system_sgpr_workgroup_id_x 1
		.amdhsa_system_sgpr_workgroup_id_y 0
		.amdhsa_system_sgpr_workgroup_id_z 0
		.amdhsa_system_sgpr_workgroup_info 0
		.amdhsa_system_vgpr_workitem_id 0
		.amdhsa_next_free_vgpr 220
		.amdhsa_next_free_sgpr 96
		.amdhsa_accum_offset 188
		.amdhsa_reserve_vcc 1
		.amdhsa_float_round_mode_32 0
		.amdhsa_float_round_mode_16_64 0
		.amdhsa_float_denorm_mode_32 3
		.amdhsa_float_denorm_mode_16_64 3
		.amdhsa_dx10_clamp 1
		.amdhsa_ieee_mode 1
		.amdhsa_fp16_overflow 0
		.amdhsa_tg_split 0
		.amdhsa_exception_fp_ieee_invalid_op 0
		.amdhsa_exception_fp_denorm_src 0
		.amdhsa_exception_fp_ieee_div_zero 0
		.amdhsa_exception_fp_ieee_overflow 0
		.amdhsa_exception_fp_ieee_underflow 0
		.amdhsa_exception_fp_ieee_inexact 0
		.amdhsa_exception_int_div_zero 0
	.end_amdhsa_kernel

amdhsa.kernels:
  - .agpr_count:     32
    .args:
      - .actual_access:  read_only
        .address_space:  global
        .offset:         0
        .size:           8
        .value_kind:     global_buffer
      - .actual_access:  read_only
        .address_space:  global
        .offset:         8
        .size:           8
        .value_kind:     global_buffer
      - .actual_access:  read_only
        .address_space:  global
        .offset:         16
        .size:           8
        .value_kind:     global_buffer
      - .actual_access:  read_only
        .address_space:  global
        .offset:         24
        .size:           8
        .value_kind:     global_buffer
      - .actual_access:  write_only
        .address_space:  global
        .offset:         32
        .size:           8
        .value_kind:     global_buffer
      - .actual_access:  write_only
        .address_space:  global
        .offset:         40
        .size:           8
        .value_kind:     global_buffer
      - .actual_access:  read_only
        .address_space:  global
        .offset:         48
        .size:           8
        .value_kind:     global_buffer
      - .actual_access:  write_only
        .address_space:  global
        .offset:         56
        .size:           8
        .value_kind:     global_buffer
    .group_segment_fixed_size: 51200
    .kernarg_segment_align: 8
    .kernarg_segment_size: 64
    .language:       OpenCL C
    .language_version:
      - 2
      - 0
    .max_flat_workgroup_size: 256
    .name:           _Z11prep_kernelPKfS0_S0_S0_PDF16_S1_S0_S1_
    .private_segment_fixed_size: 0
    .sgpr_count:     30
    .sgpr_spill_count: 0
    .symbol:         _Z11prep_kernelPKfS0_S0_S0_PDF16_S1_S0_S1_.kd
    .uniform_work_group_size: 1
    .uses_dynamic_stack: false
    .vgpr_count:     220
    .vgpr_spill_count: 0
    .wavefront_size: 64
  - .agpr_count:     0
    .args:
      - .actual_access:  read_only
        .address_space:  global
        .offset:         0
        .size:           8
        .value_kind:     global_buffer
      - .address_space:  global
        .offset:         8
        .size:           8
        .value_kind:     global_buffer
      - .actual_access:  write_only
        .address_space:  global
        .offset:         16
        .size:           8
        .value_kind:     global_buffer
      - .actual_access:  write_only
        .address_space:  global
        .offset:         24
        .size:           8
        .value_kind:     global_buffer
    .group_segment_fixed_size: 81920
    .kernarg_segment_align: 8
    .kernarg_segment_size: 32
    .language:       OpenCL C
    .language_version:
      - 2
      - 0
    .max_flat_workgroup_size: 512
    .name:           _Z11attn_kernelPKDF16_S0_PDF16_P15HIP_vector_typeIfLj2EE
    .private_segment_fixed_size: 0
    .sgpr_count:     48
    .sgpr_spill_count: 0
    .symbol:         _Z11attn_kernelPKDF16_S0_PDF16_P15HIP_vector_typeIfLj2EE.kd
    .uniform_work_group_size: 1
    .uses_dynamic_stack: false
    .vgpr_count:     244
    .vgpr_spill_count: 0
    .wavefront_size: 64
  - .agpr_count:     0
    .args:
      - .actual_access:  read_only
        .address_space:  global
        .offset:         0
        .size:           8
        .value_kind:     global_buffer
      - .actual_access:  read_only
        .address_space:  global
        .offset:         8
        .size:           8
        .value_kind:     global_buffer
      - .actual_access:  read_only
        .address_space:  global
        .offset:         16
        .size:           8
        .value_kind:     global_buffer
      - .actual_access:  read_only
        .address_space:  global
        .offset:         24
        .size:           8
        .value_kind:     global_buffer
      - .actual_access:  write_only
        .address_space:  global
        .offset:         32
        .size:           8
        .value_kind:     global_buffer
    .group_segment_fixed_size: 50176
    .kernarg_segment_align: 8
    .kernarg_segment_size: 40
    .language:       OpenCL C
    .language_version:
      - 2
      - 0
    .max_flat_workgroup_size: 256
    .name:           _Z19combine_proj_kernelPKDF16_PK15HIP_vector_typeIfLj2EES0_PKfPf
    .private_segment_fixed_size: 0
    .sgpr_count:     50
    .sgpr_spill_count: 0
    .symbol:         _Z19combine_proj_kernelPKDF16_PK15HIP_vector_typeIfLj2EES0_PKfPf.kd
    .uniform_work_group_size: 1
    .uses_dynamic_stack: false
    .vgpr_count:     220
    .vgpr_spill_count: 0
    .wavefront_size: 64
